# v24 + s_setprio 1 during the P.V pass (MFMA-only section) of both diff-attention loops
# baseline (speedup 1.0000x reference)
.LBB0_188:
	s_setprio 1
	s_waitcnt lgkmcnt(0)
	v_add_u32_e32 v0, s44, v224
	ds_read_b64_tr_b16 v[160:161], v0 offset:0
	ds_read_b64_tr_b16 v[162:163], v0 offset:0x800
	ds_read_b64_tr_b16 v[164:165], v0 offset:0x200
	ds_read_b64_tr_b16 v[166:167], v0 offset:0xa00
	ds_read_b64_tr_b16 v[168:169], v0 offset:0x400
	ds_read_b64_tr_b16 v[170:171], v0 offset:0xc00
	ds_read_b64_tr_b16 v[172:173], v0 offset:0x600
	ds_read_b64_tr_b16 v[174:175], v0 offset:0xe00
	s_waitcnt lgkmcnt(4)
	s_nop 0
	v_mfma_f32_32x32x16_bf16 v[112:127], v[208:211], v[160:163], v[112:127]
	v_mfma_f32_32x32x16_bf16 v[96:111], v[208:211], v[164:167], v[96:111]
	v_mfma_f32_32x32x16_bf16 v[128:143], v[156:159], v[160:163], v[128:143]
	v_mfma_f32_32x32x16_bf16 v[80:95], v[156:159], v[164:167], v[80:95]
	ds_read_b64_tr_b16 v[160:161], v0 offset:0x1000
	ds_read_b64_tr_b16 v[162:163], v0 offset:0x1800
	ds_read_b64_tr_b16 v[164:165], v0 offset:0x1200
	ds_read_b64_tr_b16 v[166:167], v0 offset:0x1a00
	s_waitcnt lgkmcnt(4)
	v_mfma_f32_32x32x16_bf16 v[64:79], v[208:211], v[168:171], v[64:79]
	v_mfma_f32_32x32x16_bf16 v[48:63], v[208:211], v[172:175], v[48:63]
	v_mfma_f32_32x32x16_bf16 v[32:47], v[156:159], v[168:171], v[32:47]
	v_mfma_f32_32x32x16_bf16 v[16:31], v[156:159], v[172:175], v[16:31]
	ds_read_b64_tr_b16 v[156:157], v0 offset:0x1400
	ds_read_b64_tr_b16 v[158:159], v0 offset:0x1c00
	ds_read_b64_tr_b16 v[168:169], v0 offset:0x1600
	ds_read_b64_tr_b16 v[170:171], v0 offset:0x1e00
	s_waitcnt lgkmcnt(4)
	v_mfma_f32_32x32x16_bf16 v[112:127], v[10:13], v[160:163], v[112:127]
	v_mfma_f32_32x32x16_bf16 v[96:111], v[10:13], v[164:167], v[96:111]
	v_mfma_f32_32x32x16_bf16 v[128:143], v[152:155], v[160:163], v[128:143]
	v_mfma_f32_32x32x16_bf16 v[80:95], v[152:155], v[164:167], v[80:95]
	ds_read_b64_tr_b16 v[160:161], v0 offset:0x2000
	ds_read_b64_tr_b16 v[162:163], v0 offset:0x2800
	ds_read_b64_tr_b16 v[164:165], v0 offset:0x2200
	ds_read_b64_tr_b16 v[166:167], v0 offset:0x2a00
	s_waitcnt lgkmcnt(4)
	v_mfma_f32_32x32x16_bf16 v[64:79], v[10:13], v[156:159], v[64:79]
	v_mfma_f32_32x32x16_bf16 v[48:63], v[10:13], v[168:171], v[48:63]
	v_mfma_f32_32x32x16_bf16 v[32:47], v[152:155], v[156:159], v[32:47]
	v_mfma_f32_32x32x16_bf16 v[16:31], v[152:155], v[168:171], v[16:31]
	ds_read_b64_tr_b16 v[10:11], v0 offset:0x2400
	ds_read_b64_tr_b16 v[12:13], v0 offset:0x2c00
	ds_read_b64_tr_b16 v[152:153], v0 offset:0x2600
	ds_read_b64_tr_b16 v[154:155], v0 offset:0x2e00
	s_waitcnt lgkmcnt(4)
	v_mfma_f32_32x32x16_bf16 v[112:127], v[6:9], v[160:163], v[112:127]
	v_mfma_f32_32x32x16_bf16 v[96:111], v[6:9], v[164:167], v[96:111]
	v_mfma_f32_32x32x16_bf16 v[128:143], v[148:151], v[160:163], v[128:143]
	v_mfma_f32_32x32x16_bf16 v[80:95], v[148:151], v[164:167], v[80:95]
	ds_read_b64_tr_b16 v[156:157], v0 offset:0x3000
	ds_read_b64_tr_b16 v[158:159], v0 offset:0x3800
	ds_read_b64_tr_b16 v[160:161], v0 offset:0x3200
	ds_read_b64_tr_b16 v[162:163], v0 offset:0x3a00
	s_waitcnt lgkmcnt(4)
	v_mfma_f32_32x32x16_bf16 v[64:79], v[6:9], v[10:13], v[64:79]
	v_mfma_f32_32x32x16_bf16 v[48:63], v[6:9], v[152:155], v[48:63]
	v_mfma_f32_32x32x16_bf16 v[32:47], v[148:151], v[10:13], v[32:47]
	v_mfma_f32_32x32x16_bf16 v[16:31], v[148:151], v[152:155], v[16:31]
	ds_read_b64_tr_b16 v[6:7], v0 offset:0x3400
	ds_read_b64_tr_b16 v[8:9], v0 offset:0x3c00
	ds_read_b64_tr_b16 v[10:11], v0 offset:0x3600
	ds_read_b64_tr_b16 v[12:13], v0 offset:0x3e00
	s_waitcnt lgkmcnt(4)
	v_mfma_f32_32x32x16_bf16 v[112:127], v[2:5], v[156:159], v[112:127]
	v_mfma_f32_32x32x16_bf16 v[96:111], v[2:5], v[160:163], v[96:111]
	v_mfma_f32_32x32x16_bf16 v[128:143], v[144:147], v[156:159], v[128:143]
	v_mfma_f32_32x32x16_bf16 v[80:95], v[144:147], v[160:163], v[80:95]
	s_waitcnt lgkmcnt(0)
	v_mfma_f32_32x32x16_bf16 v[64:79], v[2:5], v[6:9], v[64:79]
	v_mfma_f32_32x32x16_bf16 v[48:63], v[2:5], v[10:13], v[48:63]
	v_mfma_f32_32x32x16_bf16 v[32:47], v[144:147], v[6:9], v[32:47]
	v_mfma_f32_32x32x16_bf16 v[16:31], v[144:147], v[10:13], v[16:31]
	s_setprio 0

.LBB0_205:
	v_add_u32_e32 v219, v212, v232
	v_add_u32_e32 v212, v212, v233
	s_waitcnt lgkmcnt(0)
	v_mfma_f32_32x32x16_bf16 v[144:159], v[248:251], v[192:195], v[144:159]
	ds_read_b128 v[248:251], v219
	v_mfma_f32_32x32x16_bf16 v[160:175], v[236:239], v[192:195], v[160:175]
	ds_read_b128 v[236:239], v219 offset:8192
	v_mfma_f32_32x32x16_bf16 v[144:159], v[240:243], v[196:199], v[144:159]
	ds_read_b128 v[240:243], v212
	v_mfma_f32_32x32x16_bf16 v[160:175], v[244:247], v[196:199], v[160:175]
	ds_read_b128 v[244:247], v212 offset:8192
	s_waitcnt lgkmcnt(3)
	v_mfma_f32_32x32x16_bf16 v[144:159], v[248:251], v[200:203], v[144:159]
	s_waitcnt lgkmcnt(2)
	v_mfma_f32_32x32x16_bf16 v[160:175], v[236:239], v[200:203], v[160:175]
	v_add_f32_e32 v212, v213, v218
	v_add_f32_e32 v235, v235, v212
	s_waitcnt lgkmcnt(1)
	v_mfma_f32_32x32x16_bf16 v[144:159], v[240:243], v[204:207], v[144:159]
	s_waitcnt lgkmcnt(0)
	v_mfma_f32_32x32x16_bf16 v[160:175], v[244:247], v[204:207], v[160:175]
	s_nop 10
	v_exp_f32_e32 v212, v144
	v_exp_f32_e32 v218, v145
	v_exp_f32_e32 v242, v148
	v_exp_f32_e32 v244, v149
	v_exp_f32_e32 v213, v152
	v_exp_f32_e32 v219, v153
	v_exp_f32_e32 v243, v156
	v_exp_f32_e32 v245, v157
	v_exp_f32_e32 v236, v146
	v_exp_f32_e32 v150, v150
	v_exp_f32_e32 v248, v151
	v_exp_f32_e32 v237, v154
	v_exp_f32_e32 v151, v158
	v_exp_f32_e32 v238, v147
	v_exp_f32_e32 v239, v155
	v_exp_f32_e32 v249, v159
	v_exp_f32_e32 v160, v160
	v_exp_f32_e32 v220, v161
	v_exp_f32_e32 v164, v164
	v_exp_f32_e32 v246, v165
	v_exp_f32_e32 v161, v168
	v_exp_f32_e32 v165, v172
	v_exp_f32_e32 v221, v169
	v_exp_f32_e32 v247, v173
	v_pk_add_f32 v[144:145], v[212:213], v[218:219]
	v_pk_add_f32 v[146:147], v[242:243], v[244:245]
	v_exp_f32_e32 v162, v162
	v_exp_f32_e32 v240, v163
	v_exp_f32_e32 v166, v166
	v_exp_f32_e32 v250, v167
	v_exp_f32_e32 v163, v170
	v_exp_f32_e32 v167, v174
	v_pk_add_f32 v[144:145], v[236:237], v[144:145]
	v_pk_add_f32 v[146:147], v[150:151], v[146:147]
	v_exp_f32_e32 v241, v171
	v_exp_f32_e32 v251, v175
	v_pk_add_f32 v[144:145], v[238:239], v[144:145]
	v_pk_add_f32 v[146:147], v[248:249], v[146:147]
	v_pk_add_f32 v[144:145], v[160:161], v[144:145]
	v_pk_add_f32 v[146:147], v[164:165], v[146:147]
	v_pk_add_f32 v[144:145], v[220:221], v[144:145]
	v_pk_add_f32 v[146:147], v[246:247], v[146:147]
	v_pk_add_f32 v[144:145], v[162:163], v[144:145]
	v_pk_add_f32 v[146:147], v[166:167], v[146:147]
	v_pk_add_f32 v[144:145], v[240:241], v[144:145]
	v_pk_add_f32 v[146:147], v[250:251], v[146:147]
	v_cvt_pk_bf16_f32 v148, v213, v219
	v_pk_add_f32 v[144:145], v[144:145], v[146:147]
	v_cvt_pk_bf16_f32 v146, v242, v244
	v_pk_add_f32 v[144:145], v[144:145], v[144:145] op_sel:[0,1] op_sel_hi:[1,0]
	v_cvt_pk_bf16_f32 v147, v150, v248
	v_mov_b32_e32 v145, v144
	s_nop 1
	v_permlane32_swap_b32_e32 v144, v145
	v_add_f32_e32 v144, v144, v145
	v_add_f32_e32 v234, v234, v144
	v_cvt_pk_bf16_f32 v144, v212, v218
	v_cvt_pk_bf16_f32 v145, v236, v238
	v_cvt_pk_bf16_f32 v149, v237, v239
	v_cvt_pk_bf16_f32 v150, v243, v245
	v_cvt_pk_bf16_f32 v151, v151, v249
	v_cvt_pk_bf16_f32 v152, v160, v220
	v_cvt_pk_bf16_f32 v153, v162, v240
	v_cvt_pk_bf16_f32 v154, v164, v246
	v_cvt_pk_bf16_f32 v155, v166, v250
	v_cvt_pk_bf16_f32 v156, v161, v221
	v_cvt_pk_bf16_f32 v157, v163, v241
	v_cvt_pk_bf16_f32 v158, v165, v247
	v_cvt_pk_bf16_f32 v159, v167, v251
	v_permlane32_swap_b32_e32 v144, v146
	v_permlane32_swap_b32_e32 v145, v147
	v_permlane32_swap_b32_e32 v148, v150
	v_permlane32_swap_b32_e32 v149, v151
	v_permlane32_swap_b32_e32 v152, v154
	v_permlane32_swap_b32_e32 v153, v155
	v_permlane32_swap_b32_e32 v156, v158
	v_permlane32_swap_b32_e32 v157, v159
	s_setprio 1
	s_waitcnt lgkmcnt(0)
	v_add_u32_e32 v212, s56, v224
	ds_read_b64_tr_b16 v[160:161], v212 offset:0
	ds_read_b64_tr_b16 v[162:163], v212 offset:0x800
	ds_read_b64_tr_b16 v[164:165], v212 offset:0x200
	ds_read_b64_tr_b16 v[166:167], v212 offset:0xa00
	ds_read_b64_tr_b16 v[168:169], v212 offset:0x400
	ds_read_b64_tr_b16 v[170:171], v212 offset:0xc00
	ds_read_b64_tr_b16 v[172:173], v212 offset:0x600
	ds_read_b64_tr_b16 v[174:175], v212 offset:0xe00
	s_waitcnt lgkmcnt(4)
	s_nop 0
	v_mfma_f32_32x32x16_bf16 v[112:127], v[208:211], v[160:163], v[112:127]
	v_mfma_f32_32x32x16_bf16 v[96:111], v[208:211], v[164:167], v[96:111]
	v_mfma_f32_32x32x16_bf16 v[128:143], v[144:147], v[160:163], v[128:143]
	v_mfma_f32_32x32x16_bf16 v[80:95], v[144:147], v[164:167], v[80:95]
	ds_read_b64_tr_b16 v[160:161], v212 offset:0x1000
	ds_read_b64_tr_b16 v[162:163], v212 offset:0x1800
	ds_read_b64_tr_b16 v[164:165], v212 offset:0x1200
	ds_read_b64_tr_b16 v[166:167], v212 offset:0x1a00
	s_waitcnt lgkmcnt(4)
	v_mfma_f32_32x32x16_bf16 v[64:79], v[208:211], v[168:171], v[64:79]
	v_mfma_f32_32x32x16_bf16 v[48:63], v[208:211], v[172:175], v[48:63]
	v_mfma_f32_32x32x16_bf16 v[32:47], v[144:147], v[168:171], v[32:47]
	v_mfma_f32_32x32x16_bf16 v[16:31], v[144:147], v[172:175], v[16:31]
	ds_read_b64_tr_b16 v[144:145], v212 offset:0x1400
	ds_read_b64_tr_b16 v[146:147], v212 offset:0x1c00
	ds_read_b64_tr_b16 v[168:169], v212 offset:0x1600
	ds_read_b64_tr_b16 v[170:171], v212 offset:0x1e00
	s_waitcnt lgkmcnt(4)
	v_mfma_f32_32x32x16_bf16 v[112:127], v[10:13], v[160:163], v[112:127]
	v_mfma_f32_32x32x16_bf16 v[96:111], v[10:13], v[164:167], v[96:111]
	v_mfma_f32_32x32x16_bf16 v[128:143], v[148:151], v[160:163], v[128:143]
	v_mfma_f32_32x32x16_bf16 v[80:95], v[148:151], v[164:167], v[80:95]
	ds_read_b64_tr_b16 v[160:161], v212 offset:0x2000
	ds_read_b64_tr_b16 v[162:163], v212 offset:0x2800
	ds_read_b64_tr_b16 v[164:165], v212 offset:0x2200
	ds_read_b64_tr_b16 v[166:167], v212 offset:0x2a00
	s_waitcnt lgkmcnt(4)
	v_mfma_f32_32x32x16_bf16 v[64:79], v[10:13], v[144:147], v[64:79]
	v_mfma_f32_32x32x16_bf16 v[48:63], v[10:13], v[168:171], v[48:63]
	v_mfma_f32_32x32x16_bf16 v[32:47], v[148:151], v[144:147], v[32:47]
	v_mfma_f32_32x32x16_bf16 v[16:31], v[148:151], v[168:171], v[16:31]
	ds_read_b64_tr_b16 v[10:11], v212 offset:0x2400
	ds_read_b64_tr_b16 v[12:13], v212 offset:0x2c00
	ds_read_b64_tr_b16 v[144:145], v212 offset:0x2600
	ds_read_b64_tr_b16 v[146:147], v212 offset:0x2e00
	s_waitcnt lgkmcnt(4)
	v_mfma_f32_32x32x16_bf16 v[112:127], v[6:9], v[160:163], v[112:127]
	v_mfma_f32_32x32x16_bf16 v[96:111], v[6:9], v[164:167], v[96:111]
	v_mfma_f32_32x32x16_bf16 v[128:143], v[152:155], v[160:163], v[128:143]
	v_mfma_f32_32x32x16_bf16 v[80:95], v[152:155], v[164:167], v[80:95]
	ds_read_b64_tr_b16 v[148:149], v212 offset:0x3000
	ds_read_b64_tr_b16 v[150:151], v212 offset:0x3800
	ds_read_b64_tr_b16 v[160:161], v212 offset:0x3200
	ds_read_b64_tr_b16 v[162:163], v212 offset:0x3a00
	s_waitcnt lgkmcnt(4)
	v_mfma_f32_32x32x16_bf16 v[64:79], v[6:9], v[10:13], v[64:79]
	v_mfma_f32_32x32x16_bf16 v[48:63], v[6:9], v[144:147], v[48:63]
	v_mfma_f32_32x32x16_bf16 v[32:47], v[152:155], v[10:13], v[32:47]
	v_mfma_f32_32x32x16_bf16 v[16:31], v[152:155], v[144:147], v[16:31]
	ds_read_b64_tr_b16 v[6:7], v212 offset:0x3400
	ds_read_b64_tr_b16 v[8:9], v212 offset:0x3c00
	ds_read_b64_tr_b16 v[10:11], v212 offset:0x3600
	ds_read_b64_tr_b16 v[12:13], v212 offset:0x3e00
	s_waitcnt lgkmcnt(4)
	v_mfma_f32_32x32x16_bf16 v[112:127], v[2:5], v[148:151], v[112:127]
	v_mfma_f32_32x32x16_bf16 v[96:111], v[2:5], v[160:163], v[96:111]
	v_mfma_f32_32x32x16_bf16 v[128:143], v[156:159], v[148:151], v[128:143]
	v_mfma_f32_32x32x16_bf16 v[80:95], v[156:159], v[160:163], v[80:95]
	s_waitcnt lgkmcnt(0)
	v_mfma_f32_32x32x16_bf16 v[64:79], v[2:5], v[6:9], v[64:79]
	v_mfma_f32_32x32x16_bf16 v[48:63], v[2:5], v[10:13], v[48:63]
	v_mfma_f32_32x32x16_bf16 v[32:47], v[156:159], v[6:9], v[32:47]
	v_mfma_f32_32x32x16_bf16 v[16:31], v[156:159], v[10:13], v[16:31]
	s_setprio 0
	s_add_i32 s42, s56, 0x4000
	s_cmpk_lg_u32 s56, 0xc000
	s_cselect_b32 s56, s42, 0
	s_add_i32 s42, s90, 0x4000
	s_cmpk_lg_u32 s90, 0xc000
	s_cselect_b32 s90, s42, 0
	s_add_u32 s40, s40, 0x60000
	s_addc_u32 s41, s41, 0
	s_addk_i32 s73, 0x100
	s_add_i32 s72, s72, 64
	s_add_i32 s71, s71, 1
	s_cmpk_eq_i32 s73, 0x4000
	s_cbranch_scc1 .LBB0_220
